# speedup vs baseline: 1.0134x; 1.0071x over previous
_Z11edge_kernelPK15HIP_vector_typeIjLj2EEPKiPiPS_IiLj2EEPKfPK6__halfPfSD_:
	v_lshrrev_b32_e32 v112, 6, v0
	s_load_dwordx2 s[36:37], s[0:1], 0x20
	v_and_b32_e32 v116, 63, v0
	v_readfirstlane_b32 s38, v112
	v_lshlrev_b32_e32 v116, 4, v116
	v_mov_b32_e32 v117, 0
	s_mul_i32 s39, s2, 0x18800
	s_sub_i32 s38, s38, 2
	s_cmp_lt_i32 s38, 0
	s_cbranch_scc1 .Lq_dma_done
	s_waitcnt lgkmcnt(0)
	s_add_u32 s36, s36, s39
	s_addc_u32 s37, s37, 0
.Lq_dma_loop:
	s_lshl_b32 s40, s38, 10
	s_add_u32 s42, s36, s40
	s_addc_u32 s43, s37, 0
	s_add_i32 s41, s40, 69680
	v_lshl_add_u64 v[114:115], s[42:43], 0, v[116:117]
	s_mov_b32 m0, s41
	s_add_i32 s38, s38, 14
	global_load_lds_dwordx4 v[114:115], off
	s_cmp_lt_u32 s38, 88
	s_cbranch_scc1 .Lq_dma_loop
.Lq_dma_done:
	s_movk_i32 s3, 0x80
	v_cmp_gt_u32_e32 vcc, s3, v0
	v_mov_b32_e32 v1, 0
	s_and_saveexec_b64 s[4:5], vcc
	s_cbranch_execz .LBB1_2
	s_load_dwordx2 s[6:7], s[0:1], 0x8
	s_movk_i32 s3, 0x101
	v_mov_b32_e32 v1, s2
	v_mad_u32_u24 v2, v0, s3, v1
	v_ashrrev_i32_e32 v3, 31, v2
	s_waitcnt lgkmcnt(0)
	v_lshl_add_u64 v[2:3], v[2:3], 2, s[6:7]
	global_load_dwordx2 v[2:3], v[2:3], off
	s_movk_i32 s3, 0x186a
	v_mov_b32_e32 v1, 0x10e30
	v_lshl_add_u32 v1, v0, 2, v1
	s_waitcnt vmcnt(0)
	v_mad_u32_u24 v4, v0, s3, v2
	ds_write_b32 v1, v4
	v_sub_u32_e32 v1, v3, v2

.LBB1_128:
	s_or_b64 exec, exec, s[0:1]
	v_and_b32_e32 v4, 15, v0
	v_mov_b32_e32 v3, 0
	v_lshlrev_b32_e32 v2, 5, v4
	v_lshlrev_b32_e32 v4, 4, v4
	v_mov_b32_e32 v5, v3
	v_bfe_u32 v59, v0, 4, 2
	v_lshl_add_u64 v[40:41], s[20:21], 0, v[4:5]
	v_and_b32_e32 v4, 1, v0
	s_waitcnt lgkmcnt(0)
	v_lshlrev_b32_e32 v6, 1, v0
	v_and_b32_e32 v36, 63, v0
	v_lshl_add_u64 v[38:39], s[18:19], 0, v[2:3]
	v_cmp_eq_u32_e64 s[2:3], 1, v4
	v_and_b32_e32 v4, 28, v6
	s_waitcnt vmcnt(0)
	v_lshl_add_u64 v[44:45], s[22:23], 0, v[2:3]
	v_and_b32_e32 v2, 7, v0
	v_bitop3_b32 v69, v0, 63, v0 bitop3:0x3f
	v_lshlrev_b32_e32 v70, 11, v86
	v_lshlrev_b32_e32 v0, 5, v59
	v_mbcnt_hi_u32_b32 v75, -1, v1
	v_lshlrev_b32_e32 v2, 2, v2
	v_or3_b32 v71, v70, v0, v4
	v_lshlrev_b32_e32 v72, 2, v36
	v_and_b32_e32 v0, 64, v75
	s_barrier
	v_cmp_eq_u32_e64 s[0:1], 0, v36
	v_lshl_add_u64 v[42:43], s[8:9], 0, v[4:5]
	v_cmp_gt_u32_e64 s[4:5], 16, v36
	v_and_b32_e32 v68, 14, v6
	v_lshl_add_u64 v[46:47], s[8:9], 0, v[2:3]
	v_or_b32_e32 v37, 64, v36
	v_or_b32_e32 v73, v70, v72
	v_mov_b32_e32 v74, 0x10408
	s_mov_b32 s14, 0x3fffffc0
	v_add_u32_e32 v76, 64, v0
	v_xor_b32_e32 v77, 1, v75
	v_mov_b32_e32 v78, 0x8004
	v_xor_b32_e32 v79, 16, v75
	v_xor_b32_e32 v80, 32, v75
	v_and_b32_e32 v112, 15, v36
	v_lshlrev_b32_e32 v112, 5, v112
	s_branch .LBB1_133

.LBB1_137:
	s_or_b64 exec, exec, s[6:7]
	v_readfirstlane_b32 s10, v0
	s_cmp_ge_i32 s10, s28
	s_mov_b64 s[6:7], -1
	s_cbranch_scc1 .LBB1_132
	s_add_i32 s8, s10, s29
	s_ashr_i32 s9, s8, 31
	s_cmp_lt_u32 s10, 176
	s_cbranch_scc0 .Lq_glob
	s_lshl_b32 s6, s10, 9
	s_add_i32 s6, s6, 69680
	v_add_u32_e32 v8, s6, v112
	ds_read_b128 v[0:3], v8
	ds_read_b128 v[4:7], v8 offset:16
	s_branch .Lq_done
.Lq_glob:
	s_lshl_b64 s[6:7], s[8:9], 9
	v_lshl_add_u64 v[8:9], v[38:39], 0, s[6:7]
	global_load_dwordx4 v[0:3], v[8:9], off
	global_load_dwordx4 v[4:7], v[8:9], off offset:16
.Lq_done:
	s_lshl_b32 s6, s10, 2
	s_add_i32 s6, s6, 0x10000
	v_mov_b32_e32 v8, s6
	ds_read2_b32 v[48:49], v8 offset1:1
	v_mov_b32_e32 v81, 0
	s_waitcnt lgkmcnt(0)
	v_readfirstlane_b32 s17, v49
	v_readfirstlane_b32 s15, v48
	s_sub_i32 s16, s17, s15
	s_cmpk_lt_i32 s16, 0x41
	s_cselect_b64 s[6:7], -1, 0
	s_and_b64 vcc, exec, s[6:7]
	s_cbranch_vccnz .LBB1_146
	v_add_u32_e32 v8, s15, v59
	v_cmp_le_i32_e32 vcc, s17, v8
	s_and_saveexec_b64 s[10:11], vcc
	s_xor_b64 s[10:11], exec, s[10:11]
	s_or_saveexec_b64 s[10:11], s[10:11]
	v_mov_b32_e32 v9, 0
	s_xor_b64 exec, exec, s[10:11]
	s_cbranch_execz .LBB1_145
	v_cmp_lt_i32_e32 vcc, v77, v76
	v_lshl_add_u32 v11, v8, 3, v78
	s_mov_b64 s[12:13], 0
	v_cndmask_b32_e32 v9, v75, v77, vcc
	v_lshlrev_b32_e32 v10, 2, v9
	v_mov_b32_e32 v9, 0

	.amdhsa_kernel _Z11edge_kernelPK15HIP_vector_typeIjLj2EEPKiPiPS_IiLj2EEPKfPK6__halfPfSD_
		.amdhsa_group_segment_fixed_size 159792
		.amdhsa_private_segment_fixed_size 0
		.amdhsa_kernarg_size 64
		.amdhsa_user_sgpr_count 2
		.amdhsa_user_sgpr_dispatch_ptr 0
		.amdhsa_user_sgpr_queue_ptr 0
		.amdhsa_user_sgpr_kernarg_segment_ptr 1
		.amdhsa_user_sgpr_dispatch_id 0
		.amdhsa_user_sgpr_kernarg_preload_length 0
		.amdhsa_user_sgpr_kernarg_preload_offset 0
		.amdhsa_user_sgpr_private_segment_size 0
		.amdhsa_uses_dynamic_stack 0
		.amdhsa_enable_private_segment 0
		.amdhsa_system_sgpr_workgroup_id_x 1
		.amdhsa_system_sgpr_workgroup_id_y 0
		.amdhsa_system_sgpr_workgroup_id_z 0
		.amdhsa_system_sgpr_workgroup_info 0
		.amdhsa_system_vgpr_workitem_id 0
		.amdhsa_next_free_vgpr 128
		.amdhsa_next_free_sgpr 44
		.amdhsa_accum_offset 128
		.amdhsa_reserve_vcc 1
		.amdhsa_float_round_mode_32 0
		.amdhsa_float_round_mode_16_64 0
		.amdhsa_float_denorm_mode_32 3
		.amdhsa_float_denorm_mode_16_64 3
		.amdhsa_dx10_clamp 1
		.amdhsa_ieee_mode 1
		.amdhsa_fp16_overflow 0
		.amdhsa_tg_split 0
		.amdhsa_exception_fp_ieee_invalid_op 0
		.amdhsa_exception_fp_denorm_src 0
		.amdhsa_exception_fp_ieee_div_zero 0
		.amdhsa_exception_fp_ieee_overflow 0
		.amdhsa_exception_fp_ieee_underflow 0
		.amdhsa_exception_fp_ieee_inexact 0
		.amdhsa_exception_int_div_zero 0
	.end_amdhsa_kernel

amdhsa.kernels:
  - .agpr_count:     0
    .args:
      - .actual_access:  read_only
        .address_space:  global
        .offset:         0
        .size:           8
        .value_kind:     global_buffer
      - .actual_access:  read_only
        .address_space:  global
        .offset:         8
        .size:           8
        .value_kind:     global_buffer
      - .actual_access:  write_only
        .address_space:  global
        .offset:         16
        .size:           8
        .value_kind:     global_buffer
      - .actual_access:  write_only
        .address_space:  global
        .offset:         24
        .size:           8
        .value_kind:     global_buffer
      - .actual_access:  write_only
        .address_space:  global
        .offset:         32
        .size:           8
        .value_kind:     global_buffer
      - .actual_access:  read_only
        .address_space:  global
        .offset:         40
        .size:           8
        .value_kind:     global_buffer
      - .actual_access:  read_only
        .address_space:  global
        .offset:         48
        .size:           8
        .value_kind:     global_buffer
      - .actual_access:  read_only
        .address_space:  global
        .offset:         56
        .size:           8
        .value_kind:     global_buffer
      - .actual_access:  read_only
        .address_space:  global
        .offset:         64
        .size:           8
        .value_kind:     global_buffer
      - .actual_access:  write_only
        .address_space:  global
        .offset:         72
        .size:           8
        .value_kind:     global_buffer
      - .actual_access:  write_only
        .address_space:  global
        .offset:         80
        .size:           8
        .value_kind:     global_buffer
    .group_segment_fixed_size: 72704
    .kernarg_segment_align: 8
    .kernarg_segment_size: 88
    .language:       OpenCL C
    .language_version:
      - 2
      - 0
    .max_flat_workgroup_size: 512
    .name:           _Z9l1_kernelPKiS0_P15HIP_vector_typeIjLj2EEPiS4_PKfS6_S6_S6_PfP6__half
    .private_segment_fixed_size: 0
    .sgpr_count:     76
    .sgpr_spill_count: 0
    .symbol:         _Z9l1_kernelPKiS0_P15HIP_vector_typeIjLj2EEPiS4_PKfS6_S6_S6_PfP6__half.kd
    .uniform_work_group_size: 1
    .uses_dynamic_stack: false
    .vgpr_count:     252
    .vgpr_spill_count: 0
    .wavefront_size: 64
  - .agpr_count:     0
    .args:
      - .actual_access:  read_only
        .address_space:  global
        .offset:         0
        .size:           8
        .value_kind:     global_buffer
      - .actual_access:  read_only
        .address_space:  global
        .offset:         8
        .size:           8
        .value_kind:     global_buffer
      - .address_space:  global
        .offset:         16
        .size:           8
        .value_kind:     global_buffer
      - .address_space:  global
        .offset:         24
        .size:           8
        .value_kind:     global_buffer
      - .actual_access:  read_only
        .address_space:  global
        .offset:         32
        .size:           8
        .value_kind:     global_buffer
      - .actual_access:  read_only
        .address_space:  global
        .offset:         40
        .size:           8
        .value_kind:     global_buffer
      - .actual_access:  write_only
        .address_space:  global
        .offset:         48
        .size:           8
        .value_kind:     global_buffer
      - .actual_access:  write_only
        .address_space:  global
        .offset:         56
        .size:           8
        .value_kind:     global_buffer
    .group_segment_fixed_size: 159792
    .kernarg_segment_align: 8
    .kernarg_segment_size: 64
    .language:       OpenCL C
    .language_version:
      - 2
      - 0
    .max_flat_workgroup_size: 1024
    .name:           _Z11edge_kernelPK15HIP_vector_typeIjLj2EEPKiPiPS_IiLj2EEPKfPK6__halfPfSD_
    .private_segment_fixed_size: 0
    .sgpr_count:     50
    .sgpr_spill_count: 0
    .symbol:         _Z11edge_kernelPK15HIP_vector_typeIjLj2EEPKiPiPS_IiLj2EEPKfPK6__halfPfSD_.kd
    .uniform_work_group_size: 1
    .uses_dynamic_stack: false
    .vgpr_count:     128
    .vgpr_spill_count: 0
    .wavefront_size: 64
